# v33 + SB step 1 touches the next unit's q rows and first four K/V tiles (L2 prefetch, two dword loads per thread)
# baseline (speedup 1.0000x reference)
; #define GAS __attribute__((address_space(1)))
; #define LAS __attribute__((address_space(3)))
; #define GAS __attribute__((address_space(1)))
; #define SB_ISSUE(j) do { int kt_ = kt_hi - (j); kt_ = kt_ < 0 ? 0 : kt_; LAS unsigned char* sl_ = lds + ((j) % NS) * 16384 + wid * 1024; \
;         dma16(ksrc + (size_t)kt_ * 64 * 1536, sl_); dma16(vsrc + (size_t)kt_ * 64 * 1536, sl_ + 8192); } while (0)
; __device__ __forceinline__ void sb_unit(LAS unsigned char* lds, int tid, const bf16_t* QKV, bf16_t* OA, float* OSS, int b, int h, int qb) {
;     ...
;     const int lane = tid & 63, r32 = lane & 31, hi = lane >> 5, wid = __builtin_amdgcn_readfirstlane(tid >> 6);
;     const size_t rowb = (size_t)b * SEQ; const int q0 = qb * 256;
;     const bf16_t* Qw = QKV + (rowb + q0 + wid * 32) * 1536 + h * 64;
;     const bf16_t* Kh = QKV + rowb * 1536 + 512 + h * 64; const bf16_t* Vh = Kh + 512;
;     const int kt_hi = (q0 >> 6) + 3, NT = kt_hi + 1, jd = 3 - (wid >> 1);
;     const bf16_t* ksrc = Kh + (size_t)lane * 1536 + wid * 8;
;     const bf16_t* vsrc = Vh + (size_t)(16 * (wid & 3) + (lane >> 2)) * 1536 + (wid >> 2) * 32 + (lane & 3) * 8;
;     ...
;     bf16x8 qr[4];
; #pragma unroll
;     for (int d0 = 0; d0 < 4; ++d0) qr[d0] = *(const GAS bf16x8*)(Qw + (size_t)r32 * 1536 + d0 * 16 + hi * 8);
; #pragma unroll
;     for (int j = 0; j < PF; ++j) SB_ISSUE(j);
;     asm volatile("" : "+v"(qr[0]), "+v"(qr[1]), "+v"(qr[2]), "+v"(qr[3]));
;     f32x16 o0 = {}, o1 = {}; float carry = 1.f; bool mydone = false;
;     const int q = q0 + wid * 32 + r32;
;     volatile LAS unsigned* flags = (volatile LAS unsigned*)(lds + FLAG_OFF);
;     const int vpo = ((lane >> 4) & 1) * 32 + (lane & 3) * 8 + (4 * hi + ((lane & 15) >> 2)) * 64;
.LBB0_876:
	v_mov_b32_e32 v8, v188
	s_ashr_i32 s8, s79, 7
	s_and_b32 s2, s78, 15
	v_readfirstlane_b32 s13, v8
	s_and_b32 s12, s79, 15
	s_ashr_i32 s14, s13, 6
	s_ashr_i32 s9, s8, 31
	s_lshl_b32 s95, s2, 2
	s_lshl_b64 s[90:91], s[8:9], 12
	s_lshl_b32 s2, s12, 8
	s_lshl_b32 s3, s14, 5
	s_bfe_u32 s94, s79, 0x30004
	v_writelane_b32 v255, s2, 42
	s_or_b32 s2, s90, s2
	s_ashr_i32 s6, s3, 31
	s_add_u32 s2, s2, s3
	s_addc_u32 s6, s91, s6
	s_mulk_i32 s6, 0xc00
	s_mul_hi_u32 s7, s2, 0xc00
	s_add_i32 s7, s7, s6
	s_mulk_i32 s2, 0xc00
	v_readlane_b32 s10, v255, 40
	s_add_u32 s2, s10, s2
	v_readlane_b32 s11, v255, 41
	s_waitcnt vmcnt(0)
	v_and_b32_e32 v115, 31, v8
	s_addc_u32 s7, s11, s7
	s_lshl_b32 s6, s94, 6
	s_lshl_b32 s9, s94, 7
	v_writelane_b32 v255, s6, 43
	s_add_u32 s6, s2, s9
	v_mul_u32_u24_e32 v0, 0x600, v115
	v_bfe_u32 v9, v8, 5, 1
	s_addc_u32 s7, s7, 0
	v_lshlrev_b32_e32 v0, 1, v0
	v_lshl_add_u64 v[2:3], s[6:7], 0, v[0:1]
	v_lshlrev_b32_e32 v0, 4, v9
	v_lshl_add_u64 v[2:3], v[2:3], 0, v[0:1]
	global_load_dwordx4 v[66:69], v[2:3], off offset:96
	global_load_dwordx4 v[70:73], v[2:3], off offset:64
	global_load_dwordx4 v[74:77], v[2:3], off offset:32
	global_load_dwordx4 v[78:81], v[2:3], off
	v_mov_b32_e32 v240, v2
	v_mov_b32_e32 v241, v3
	s_mul_i32 s7, s8, 0xc00000
	s_mul_hi_i32 s6, s8, 0xc00000
	s_add_u32 s7, s10, s7
	s_addc_u32 s8, s11, s6
	s_add_u32 s6, s7, s9
	s_waitcnt lgkmcnt(8)
	v_and_b32_e32 v120, 63, v8
	s_addc_u32 s7, s8, 0
	s_lshl_b32 s10, s14, 4
	v_bfe_u32 v2, v8, 2, 4
	v_mul_u32_u24_e32 v0, 0x600, v120
	v_and_or_b32 v2, s10, 48, v2
	s_lshl_b32 s82, s12, 2
	s_lshl_b32 s8, s14, 3
	v_mul_u32_u24_e32 v4, 0x600, v2
	s_ashr_i32 s10, s13, 3
	v_lshlrev_b32_e32 v2, 3, v8
	v_lshlrev_b32_e32 v0, 1, v0
	s_ashr_i32 s9, s8, 31
	s_andn2_b32 s10, s10, 31
	v_and_b32_e32 v10, 24, v2
	s_or_b32 s15, s82, 3
	v_lshl_add_u64 v[2:3], s[6:7], 0, v[0:1]
	v_lshlrev_b32_e32 v0, 1, v4
	s_ashr_i32 s11, s10, 31
	v_lshl_add_u64 v[116:117], s[8:9], 1, v[2:3]
	v_lshl_add_u64 v[4:5], s[6:7], 0, v[0:1]
	s_mul_i32 s88, s15, 0x30000
	v_lshl_add_u64 v[4:5], s[10:11], 1, v[4:5]
	v_lshlrev_b32_e32 v0, 1, v10
	s_lshl_b32 s6, s14, 10
	v_lshl_add_u64 v[6:7], v[116:117], 0, s[88:89]
	v_lshl_add_u64 v[118:119], v[4:5], 0, v[0:1]
	s_add_i32 s33, s6, 0
	v_lshl_add_u64 v[6:7], v[6:7], 0, s[28:29]
	s_mov_b32 s6, m0
	s_mov_b32 m0, s33
	s_nop 0
	global_load_lds_dwordx4 v[6:7], off
	s_mov_b32 m0, s6
	v_lshl_add_u64 v[6:7], v[118:119], 0, s[88:89]
	s_add_i32 s6, s33, 0x2000
	v_lshl_add_u64 v[6:7], v[6:7], 0, s[30:31]
	s_mov_b32 s7, m0
	s_mov_b32 m0, s6
	s_nop 0
	global_load_lds_dwordx4 v[6:7], off
	s_mov_b32 m0, s7
	s_mul_i32 s6, s12, 0xc0000
	v_lshl_add_u64 v[2:3], v[116:117], 0, s[28:29]
	s_add_i32 s7, s33, 0x4000
	s_add_i32 s88, s6, 0x60000
	v_lshl_add_u64 v[4:5], v[118:119], 0, s[30:31]
	v_lshl_add_u64 v[6:7], v[2:3], 0, s[88:89]
	s_mov_b32 s8, m0
	s_mov_b32 m0, s7
	s_nop 0
	global_load_lds_dwordx4 v[6:7], off
	s_mov_b32 m0, s8
	s_add_i32 s7, s33, 0x6000
	v_lshl_add_u64 v[6:7], v[4:5], 0, s[88:89]
	s_mov_b32 s8, m0
	s_mov_b32 m0, s7
	s_nop 0
	global_load_lds_dwordx4 v[6:7], off
	s_mov_b32 m0, s8
	s_add_i32 s7, s33, 0x8000
	s_or_b32 s88, s6, 0x30000
	v_lshl_add_u64 v[2:3], v[2:3], 0, s[88:89]
	s_mov_b32 s8, m0
	s_mov_b32 m0, s7
	s_nop 0
	global_load_lds_dwordx4 v[2:3], off
	s_mov_b32 m0, s8
	s_add_i32 s7, s33, 0xa000
	v_lshl_add_u64 v[2:3], v[4:5], 0, s[88:89]
	s_mov_b32 s8, m0
	s_mov_b32 m0, s7
	s_nop 0
	global_load_lds_dwordx4 v[2:3], off
	s_mov_b32 m0, s8
	s_mov_b32 s7, s89
	v_lshl_add_u64 v[2:3], v[116:117], 0, s[6:7]
	v_lshl_add_u64 v[2:3], v[2:3], 0, s[28:29]
	s_add_i32 s8, s33, 0xc000
	s_mov_b32 s9, m0
	s_mov_b32 m0, s8
	s_nop 0
	global_load_lds_dwordx4 v[2:3], off
	s_mov_b32 m0, s9
	v_lshl_add_u64 v[2:3], v[118:119], 0, s[6:7]
	v_lshl_add_u64 v[2:3], v[2:3], 0, s[30:31]
	s_add_i32 s6, s33, 0xe000
	s_mov_b32 s7, m0
	s_mov_b32 m0, s6
	s_nop 0
	global_load_lds_dwordx4 v[2:3], off
	s_mov_b32 m0, s7
	v_sub_u32_e64 v0, s82, 1 clamp
	s_mov_b32 s7, 0x30000
	v_mul_lo_u32 v0, v0, s7
	v_lshl_add_u64 v[2:3], v[116:117], 0, v[0:1]
	v_lshl_add_u64 v[2:3], v[2:3], 0, s[28:29]
	s_add_i32 s6, s33, 0x10000
	s_mov_b32 s7, m0
	s_mov_b32 m0, s6
	s_nop 0
	global_load_lds_dwordx4 v[2:3], off
	s_mov_b32 m0, s7
	v_lshl_add_u64 v[2:3], v[118:119], 0, v[0:1]
	v_lshl_add_u64 v[2:3], v[2:3], 0, s[30:31]
	s_add_i32 s6, s33, 0x12000
	s_mov_b32 s7, m0
	s_mov_b32 m0, s6
	s_nop 0
	global_load_lds_dwordx4 v[2:3], off
	s_mov_b32 m0, s7
	v_lshlrev_b32_e32 v2, 4, v8
	v_lshlrev_b32_e32 v0, 1, v8
	v_and_b32_e32 v2, 0xc0, v2
	v_and_b32_e32 v0, 32, v0
	v_lshl_or_b32 v2, v9, 8, v2
	s_ashr_i32 s6, s13, 7
	v_or3_b32 v121, v2, v0, v10
	s_lshl_b32 s7, s14, 2
	v_lshlrev_b32_e32 v0, 2, v9
	v_or_b32_e32 v2, s3, v115
	s_add_i32 s88, s7, 0
	v_sub_u32_e32 v0, v2, v0
	s_lshl_b32 s7, s6, 6
	v_mov_b32_e32 v14, v1
	v_mov_b32_e32 v15, v1
	v_lshlrev_b32_e32 v114, 3, v9
	v_lshlrev_b32_e32 v123, 10, v9
	v_subrev_u32_e32 v124, s7, v0
	v_mov_b32_e32 v0, v1
	v_mov_b32_e32 v2, v1
	v_mov_b32_e32 v3, v1
	v_mov_b32_e32 v4, v1
	v_mov_b32_e32 v5, v1
	v_mov_b32_e32 v6, v1
	v_mov_b32_e32 v7, v1
	v_mov_b32_e32 v8, v1
	v_mov_b32_e32 v9, v1
	v_mov_b32_e32 v10, v1
	v_mov_b32_e32 v11, v1
	v_mov_b32_e32 v12, v1
	v_mov_b32_e32 v13, v1
	v_mov_b64_e32 v[32:33], v[14:15]
	v_mov_b64_e32 v[30:31], v[12:13]
	v_mov_b64_e32 v[28:29], v[10:11]
	v_mov_b64_e32 v[26:27], v[8:9]
	v_mov_b64_e32 v[24:25], v[6:7]
	v_mov_b64_e32 v[22:23], v[4:5]
	v_mov_b64_e32 v[20:21], v[2:3]
	v_mov_b64_e32 v[18:19], v[0:1]
	v_mov_b64_e32 v[16:17], v[14:15]
	s_mov_b32 s2, 5
	s_add_i32 s83, s82, 4
	s_add_i32 s88, s88, 0x20200
	v_lshlrev_b32_e32 v122, 4, v115
	s_mov_b32 s81, 0
	v_cmp_eq_u32_e64 s[8:9], 0, v120
	s_add_i32 s76, s95, 4
	s_sub_i32 s97, 0, s6
	v_mov_b32_e32 v125, 1.0
	s_mov_b64 s[10:11], 0
	s_mov_b32 s80, -2
	s_mov_b32 s77, 0
	s_mov_b32 s6, 0
	v_mov_b64_e32 v[14:15], v[12:13]
	v_mov_b64_e32 v[12:13], v[10:11]
	v_mov_b64_e32 v[10:11], v[8:9]
	v_mov_b64_e32 v[8:9], v[6:7]
	v_mov_b64_e32 v[6:7], v[4:5]
	v_mov_b64_e32 v[4:5], v[2:3]
	v_mov_b64_e32 v[2:3], v[0:1]
	s_waitcnt vmcnt(0)
	s_branch .LBB0_878

; template <bool DIAG> __device__ __forceinline__ void sb_tile(const LAS unsigned char* ks, int vpo, const bf16x8 (&qr)[4], f32x16& o0, f32x16& o1, float& carry, int kb, int q, int r32, int hi) {
;     f32x16 z0 = {}, z1 = {};
;     bf16x8 kf[8], vf[8];
; #pragma unroll
;     for (int d0 = 0; d0 < 4; ++d0) { kf[2 * d0] = *(const LAS bf16x8*)(ks + (2 * d0 + hi) * 1024 + r32 * 16); kf[2 * d0 + 1] = *(const LAS bf16x8*)(ks + (2 * d0 + hi) * 1024 + 512 + r32 * 16); }
;     __builtin_amdgcn_sched_barrier(0);
; #pragma unroll
;     for (int d0 = 0; d0 < 4; ++d0) { z0 = __builtin_amdgcn_mfma_f32_32x32x16_bf16(kf[2 * d0], qr[d0], z0, 0, 0, 0); z1 = __builtin_amdgcn_mfma_f32_32x32x16_bf16(kf[2 * d0 + 1], qr[d0], z1, 0, 0, 0); }
;     v_load(vf, ks + 8192 + vpo);
;     __builtin_amdgcn_sched_barrier(0);
;     f32x16 s0, s1;
; #pragma unroll
;     for (int r = 0; r < 16; ++r) { s0[r] = frcp(1.f + fexp2(z0[r])); s1[r] = frcp(1.f + fexp2(z1[r])); }
;     asm volatile("s_nop 0" : "+v"(s0), "+v"(s1));
;     if (DIAG) {
;         const int dq = q - kb - 4 * hi;
; #pragma unroll
;         for (int r = 0; r < 16; ++r) { if (crow(r, 0) >= dq) s0[r] = 1.f; if (32 + crow(r, 0) >= dq) s1[r] = 1.f; }
;     }
; #pragma unroll
;     for (int g = 0; g < 4; ++g) {
;         s0[4 * g + 2] = vmul(s0[4 * g + 2], s0[4 * g + 3]); s0[4 * g + 1] = vmul(s0[4 * g + 1], s0[4 * g + 2]); s0[4 * g] = vmul(s0[4 * g], s0[4 * g + 1]);
;         s1[4 * g + 2] = vmul(s1[4 * g + 2], s1[4 * g + 3]); s1[4 * g + 1] = vmul(s1[4 * g + 1], s1[4 * g + 2]); s1[4 * g] = vmul(s1[4 * g], s1[4 * g + 1]);
;     }
; __device__ __forceinline__ void sb_unit(LAS unsigned char* lds, int tid, const bf16_t* QKV, bf16_t* OA, float* OSS, int b, int h, int qb) {
;     ...
;     for (int j = 0; j < NT; ++j) {
;         ATT_WAIT_BAR(2);
;         if (j >= 1) { const u32x4 fa = *(const LAS u32x4*)(lds + FLAG_OFF + ((j - 1) & 1) * 32), fb = *(const LAS u32x4*)(lds + FLAG_OFF + ((j - 1) & 1) * 32 + 16);
;             if ((fa.x & fa.y & fa.z & fa.w & fb.x & fb.y & fb.z & fb.w) != 0u) break; }
;         SB_ISSUE(j + PF);
;         const int tj = j + jd;
;         if (tj < NT && !mydone) {
;             const LAS unsigned char* ks = lds + (tj % NS) * 16384; const int kb = (kt_hi - tj) * 64;
;             if (j == 0) sb_tile<true>(ks, vpo, qr, o0, o1, carry, kb, q, r32, hi); else sb_tile<false>(ks, vpo, qr, o0, o1, carry, kb, q, r32, hi);
.LBB0_880:
	s_andn2_b64 vcc, exec, s[14:15]
	s_cbranch_vccnz .LBB0_877
	s_cmp_lg_u32 s6, 1
	s_cbranch_scc1 .Lsbq_nopf
	s_add_i32 s14, s79, s76
	s_cmpk_ge_i32 s14, 0x400
	s_cbranch_scc1 .Lsbq_nopf
	v_bfe_u32 v242, v188, 5, 1
	v_lshlrev_b32_e32 v242, 10, v242
	v_add_co_u32_e32 v242, vcc, v240, v242
	v_addc_co_u32_e32 v243, vcc, 0, v241, vcc
	v_add_co_u32_e32 v242, vcc, 0x1800000, v242
	s_nop 1
	v_addc_co_u32_e32 v243, vcc, 0, v243, vcc
	global_load_dword v244, v[242:243], off
	global_load_dword v245, v[242:243], off offset:2048
.Lsbq_nopf:
	s_mul_hi_u32 s7, s2, 0xaaaaaaab
	s_add_i32 s14, s95, s80
	s_lshr_b32 s7, s7, 2
	s_max_i32 s16, s14, 0
	s_mul_i32 s7, s7, 0xfffe8000
	v_mad_u64_u32 v[34:35], s[14:15], s16, v234, v[116:117]
	s_add_i32 s7, s33, s7
	v_lshl_add_u64 v[34:35], v[34:35], 0, s[28:29]
	s_add_i32 s17, s7, 0x14000
	s_mov_b32 s14, m0
	s_mov_b32 m0, s17
	s_nop 0
	global_load_lds_dwordx4 v[34:35], off
	s_mov_b32 m0, s14
	s_add_i32 s7, s7, 0x16000
	v_mad_u64_u32 v[34:35], s[14:15], s16, v234, v[118:119]
	v_lshl_add_u64 v[34:35], v[34:35], 0, s[30:31]
	s_mov_b32 s14, m0
	s_mov_b32 m0, s7
	s_nop 0
	global_load_lds_dwordx4 v[34:35], off
	s_mov_b32 m0, s14
	s_add_i32 s7, s97, s6
	s_add_i32 s14, s7, 3
	s_cmp_ge_i32 s14, s83
	s_cselect_b64 s[16:17], -1, 0
	s_or_b64 s[10:11], s[16:17], s[10:11]
	s_and_b64 vcc, exec, s[10:11]
	s_cbranch_vccnz .LBB0_887
	s_mul_hi_i32 s10, s14, 0x2aaaaaab
	s_lshr_b32 s11, s10, 31
	s_add_i32 s10, s10, s11
	s_mul_i32 s10, s10, 6
	s_sub_i32 s10, s14, s10
	s_lshl_b32 s10, s10, 14
	s_add_i32 s14, s10, 0
	v_add_u32_e32 v0, s14, v121
	s_mov_b64 s[10:11], -1
	s_and_b64 vcc, exec, s[12:13]
	v_add3_u32 v126, s14, v123, v122
	v_add_u32_e32 v0, 0x2000, v0
	s_cbranch_vccz .LBB0_884
	ds_read_b128 v[34:37], v126
	ds_read_b128 v[50:53], v126 offset:512
	ds_read_b128 v[82:85], v126 offset:2048
	ds_read_b128 v[86:89], v126 offset:2560
	ds_read_b128 v[90:93], v126 offset:4096
	ds_read_b128 v[94:97], v126 offset:4608
	ds_read_b128 v[98:101], v126 offset:6144
	ds_read_b128 v[102:105], v126 offset:6656
	s_waitcnt lgkmcnt(7)
	v_mfma_f32_32x32x16_bf16 v[34:49], v[34:37], v[78:81], 0
	ds_read_b64_tr_b16 v[110:111], v0 offset:0
	ds_read_b64_tr_b16 v[112:113], v0 offset:512
	ds_read_b64_tr_b16 v[106:107], v0 offset:4096
	ds_read_b64_tr_b16 v[108:109], v0 offset:4608
	s_waitcnt lgkmcnt(6)
	v_mfma_f32_32x32x16_bf16 v[50:65], v[50:53], v[78:81], 0
	s_waitcnt lgkmcnt(5)
	v_mfma_f32_32x32x16_bf16 v[34:49], v[82:85], v[74:77], v[34:49]
	s_waitcnt lgkmcnt(4)
	v_mfma_f32_32x32x16_bf16 v[50:65], v[86:89], v[74:77], v[50:65]
	s_waitcnt lgkmcnt(3)
	v_mfma_f32_32x32x16_bf16 v[34:49], v[90:93], v[70:73], v[34:49]
	s_waitcnt lgkmcnt(2)
	v_mfma_f32_32x32x16_bf16 v[50:65], v[94:97], v[70:73], v[50:65]
	s_waitcnt lgkmcnt(1)
	v_mfma_f32_32x32x16_bf16 v[34:49], v[98:101], v[66:69], v[34:49]
	s_waitcnt lgkmcnt(0)
	v_mfma_f32_32x32x16_bf16 v[50:65], v[102:105], v[66:69], v[50:65]
	ds_read_b64_tr_b16 v[102:103], v0 offset:1024
	ds_read_b64_tr_b16 v[104:105], v0 offset:1536
	ds_read_b64_tr_b16 v[98:99], v0 offset:5120
	ds_read_b64_tr_b16 v[100:101], v0 offset:5632
	ds_read_b64_tr_b16 v[94:95], v0 offset:2048
	ds_read_b64_tr_b16 v[96:97], v0 offset:2560
	ds_read_b64_tr_b16 v[90:91], v0 offset:6144
	ds_read_b64_tr_b16 v[92:93], v0 offset:6656
	ds_read_b64_tr_b16 v[86:87], v0 offset:3072
	ds_read_b64_tr_b16 v[88:89], v0 offset:3584
	ds_read_b64_tr_b16 v[82:83], v0 offset:7168
	ds_read_b64_tr_b16 v[84:85], v0 offset:7680
	s_nop 9
	v_exp_f32_e32 v34, v34
	s_nop 0
	v_exp_f32_e32 v50, v50
	v_exp_f32_e32 v35, v35
	v_exp_f32_e32 v51, v51
	v_exp_f32_e32 v36, v36
	v_exp_f32_e32 v52, v52
	v_exp_f32_e32 v37, v37
	v_exp_f32_e32 v53, v53
	v_exp_f32_e32 v38, v38
	v_exp_f32_e32 v54, v54
	v_exp_f32_e32 v39, v39
	v_exp_f32_e32 v55, v55
	v_exp_f32_e32 v40, v40
	v_exp_f32_e32 v56, v56
	v_exp_f32_e32 v41, v41
	v_exp_f32_e32 v57, v57
	v_exp_f32_e32 v42, v42
	v_exp_f32_e32 v58, v58
	v_exp_f32_e32 v43, v43
	v_exp_f32_e32 v59, v59
	v_exp_f32_e32 v44, v44
	v_exp_f32_e32 v60, v60
	v_exp_f32_e32 v45, v45
	v_exp_f32_e32 v61, v61
	v_exp_f32_e32 v46, v46
	v_exp_f32_e32 v62, v62
	v_exp_f32_e32 v47, v47
	v_exp_f32_e32 v63, v63
	v_exp_f32_e32 v48, v48
	v_exp_f32_e32 v64, v64
	v_exp_f32_e32 v49, v49
	v_exp_f32_e32 v65, v65
	v_add_f32_e32 v34, 1.0, v34
	v_add_f32_e32 v50, 1.0, v50
	v_add_f32_e32 v35, 1.0, v35
	v_add_f32_e32 v51, 1.0, v51
	v_add_f32_e32 v36, 1.0, v36
	v_add_f32_e32 v52, 1.0, v52
	v_add_f32_e32 v37, 1.0, v37
	v_add_f32_e32 v53, 1.0, v53
	v_add_f32_e32 v38, 1.0, v38
	v_add_f32_e32 v54, 1.0, v54
	v_add_f32_e32 v39, 1.0, v39
	v_add_f32_e32 v55, 1.0, v55
	v_add_f32_e32 v40, 1.0, v40
	v_add_f32_e32 v56, 1.0, v56
	v_add_f32_e32 v41, 1.0, v41
	v_add_f32_e32 v57, 1.0, v57
	v_add_f32_e32 v42, 1.0, v42
	v_add_f32_e32 v58, 1.0, v58
	v_add_f32_e32 v43, 1.0, v43
	v_add_f32_e32 v59, 1.0, v59
	v_add_f32_e32 v44, 1.0, v44
	v_add_f32_e32 v60, 1.0, v60
	v_add_f32_e32 v45, 1.0, v45
	v_add_f32_e32 v61, 1.0, v61
	v_add_f32_e32 v46, 1.0, v46
	v_add_f32_e32 v62, 1.0, v62
	v_add_f32_e32 v47, 1.0, v47
	v_add_f32_e32 v63, 1.0, v63
	v_add_f32_e32 v48, 1.0, v48
	v_add_f32_e32 v64, 1.0, v64
	v_add_f32_e32 v49, 1.0, v49
	v_add_f32_e32 v65, 1.0, v65
	v_rcp_f32_e32 v34, v34
	v_rcp_f32_e32 v50, v50
	v_rcp_f32_e32 v35, v35
	v_rcp_f32_e32 v51, v51
	v_rcp_f32_e32 v36, v36
	v_rcp_f32_e32 v52, v52
	v_rcp_f32_e32 v37, v37
	v_rcp_f32_e32 v53, v53
	v_rcp_f32_e32 v38, v38
	v_rcp_f32_e32 v54, v54
	v_rcp_f32_e32 v39, v39
	v_rcp_f32_e32 v55, v55
	v_rcp_f32_e32 v40, v40
	v_rcp_f32_e32 v56, v56
	v_rcp_f32_e32 v41, v41
	v_rcp_f32_e32 v57, v57
	v_rcp_f32_e32 v42, v42
	v_rcp_f32_e32 v58, v58
	v_rcp_f32_e32 v43, v43
	v_rcp_f32_e32 v59, v59
	v_rcp_f32_e32 v44, v44
	v_rcp_f32_e32 v60, v60
	v_rcp_f32_e32 v45, v45
	v_rcp_f32_e32 v61, v61
	v_rcp_f32_e32 v46, v46
	v_rcp_f32_e32 v62, v62
	v_rcp_f32_e32 v47, v47
	v_rcp_f32_e32 v63, v63
	v_rcp_f32_e32 v48, v48
	v_rcp_f32_e32 v64, v64
	v_rcp_f32_e32 v49, v49
	v_rcp_f32_e32 v65, v65
	s_nop 0
	v_mov_b32_e32 v136, 1.0
	v_mul_f32 v36, v36, v37
	v_mul_f32 v52, v52, v53
	v_mul_f32 v40, v40, v41
	v_mul_f32 v56, v56, v57
	v_mul_f32 v44, v44, v45
	v_mul_f32 v60, v60, v61
	s_nop 0
	v_mul_f32 v35, v35, v36
	v_mul_f32 v51, v51, v52
	v_mul_f32 v39, v39, v40
	v_mul_f32 v55, v55, v56
	v_mul_f32 v43, v43, v44
	v_mul_f32 v59, v59, v60
	s_nop 0
	v_mul_f32 v34, v34, v35
	v_mul_f32 v50, v50, v51
	v_mul_f32 v38, v38, v39
	v_mul_f32 v54, v54, v55
	v_mul_f32 v42, v42, v43
	v_mul_f32 v58, v58, v59
	v_mul_f32 v48, v48, v49
	v_mul_f32 v64, v64, v65
	s_waitcnt lgkmcnt(0)
; __device__ __forceinline__ float vmul(float a, float b) { float r; asm("v_mul_f32 %0, %1, %2" : "=v"(r) : "v"(a), "v"(b)); return r; }
; __device__ __forceinline__ float vsub(float a, float b) { float r; asm("v_sub_f32 %0, %1, %2" : "=v"(r) : "v"(a), "v"(b)); return r; }
; __device__ __forceinline__ void pv_tile(f32x16& o0, f32x16& o1, const bf16x8 (&vf)[8], const f32x16& w0, const f32x16& w1) {
; #pragma unroll
;     for (int ks = 0; ks < 4; ++ks) {
;         const bf16x8 pf = pfrag(ks < 2 ? w0 : w1, 8 * (ks & 1));
;         o0 = __builtin_amdgcn_mfma_f32_32x32x16_bf16(vf[2 * ks], pf, o0, 0, 0, 0);
;         o1 = __builtin_amdgcn_mfma_f32_32x32x16_bf16(vf[2 * ks + 1], pf, o1, 0, 0, 0);
;     }
; template <bool DIAG> __device__ __forceinline__ void sb_tile(const LAS unsigned char* ks, int vpo, const bf16x8 (&qr)[4], f32x16& o0, f32x16& o1, float& carry, int kb, int q, int r32, int hi) {
;     ...
;         s0[4 * g + 2] = vmul(s0[4 * g + 2], s0[4 * g + 3]); s0[4 * g + 1] = vmul(s0[4 * g + 1], s0[4 * g + 2]); s0[4 * g] = vmul(s0[4 * g], s0[4 * g + 1]);
;         s1[4 * g + 2] = vmul(s1[4 * g + 2], s1[4 * g + 3]); s1[4 * g + 1] = vmul(s1[4 * g + 1], s1[4 * g + 2]); s1[4 * g] = vmul(s1[4 * g], s1[4 * g + 1]);
;     }
;     float I[9]; I[8] = 1.f; I[7] = s1[12];
; #pragma unroll
;     for (int g = 6; g >= 0; --g) I[g] = vmul(I[g + 1], g < 4 ? s0[4 * g] : s1[4 * (g - 4)]);
;     float off[8];
; #pragma unroll
;     for (int g = 0; g < 8; ++g) {
;         const float x = swap_sel(I[g], I[g + 1]);
;         off[g] = (g == 7) ? vmul(carry, x) : vmul(vmul(carry, I[g + 1]), x);
;     }
;     carry = vmul(carry, vmul(I[0], swap32(I[0])));
;     f32x16 w0, w1;
; #pragma unroll
;     for (int g = 0; g < 4; ++g) {
;         { const float o = off[g]; const float S3 = vmul(s0[4 * g + 3], o), S2 = vmul(s0[4 * g + 2], o), S1 = vmul(s0[4 * g + 1], o), S0 = vmul(s0[4 * g], o);
;           w0[4 * g + 3] = vsub(o, S3); w0[4 * g + 2] = vsub(S3, S2); w0[4 * g + 1] = vsub(S2, S1); w0[4 * g] = vsub(S1, S0); }
;         { const float o = off[4 + g]; const float S3 = vmul(s1[4 * g + 3], o), S2 = vmul(s1[4 * g + 2], o), S1 = vmul(s1[4 * g + 1], o), S0 = vmul(s1[4 * g], o);
;           w1[4 * g + 3] = vsub(o, S3); w1[4 * g + 2] = vsub(S3, S2); w1[4 * g + 1] = vsub(S2, S1); w1[4 * g] = vsub(S1, S0); }
;     }
;     V_WAIT(vf);
;     pv_tile(o0, o1, vf, w0, w1);
	s_mov_b64 s[10:11], 0
	v_mul_f32 v47, v47, v48
	v_mul_f32 v63, v63, v64
	s_nop 0
	v_mul_f32 v46, v46, v47
	v_mul_f32 v62, v62, v63
	s_nop 0
	v_mul_f32 v127, v62, v58
	s_nop 0
	v_mul_f32 v128, v127, v54
	s_nop 0
	v_mul_f32 v129, v128, v50
	s_nop 0
	v_mul_f32 v130, v129, v46
	s_nop 0
	v_mul_f32 v131, v130, v42
	s_nop 0
	v_mul_f32 v132, v131, v38
	s_nop 0
	v_mul_f32 v133, v132, v34
	v_mov_b32_e32 v134, v132
	v_mov_b32_e32 v135, v133
	s_nop 1
	v_permlane32_swap_b32_e32 v135, v134
	v_cndmask_b32_e64 v134, v135, v134, s[4:5]
	v_mul_f32 v135, v125, v132
	v_mov_b32_e32 v137, v133
	v_mul_f32 v134, v135, v134
	v_mov_b32_e32 v135, v131
	s_nop 1
	v_permlane32_swap_b32_e32 v132, v135
	v_cndmask_b32_e64 v132, v132, v135, s[4:5]
	v_mul_f32 v135, v125, v131
	v_mul_f32 v37, v37, v134
	v_mul_f32 v36, v36, v134
	v_mul_f32 v35, v35, v134
	v_mul_f32 v34, v34, v134
	s_nop 0
	v_mul_f32 v132, v135, v132
	v_mov_b32_e32 v135, v130
	s_nop 1
	v_permlane32_swap_b32_e32 v131, v135
	v_cndmask_b32_e64 v131, v131, v135, s[4:5]
	v_mul_f32 v135, v125, v130
	v_sub_f32 v34, v35, v34
	v_mul_f32 v40, v40, v132
	v_mul_f32 v39, v39, v132
	v_mul_f32 v38, v38, v132
	s_nop 0
	v_mul_f32 v131, v135, v131
	v_mov_b32_e32 v135, v129
	s_nop 1
	v_permlane32_swap_b32_e32 v130, v135
	v_cndmask_b32_e64 v130, v130, v135, s[4:5]
	v_mul_f32 v135, v125, v129
	v_sub_f32 v38, v39, v38
	v_mul_f32 v44, v44, v131
	v_mul_f32 v43, v43, v131
	v_mul_f32 v42, v42, v131
	s_nop 0
	v_mul_f32 v130, v135, v130
	v_mov_b32_e32 v135, v128
	s_nop 1
	v_permlane32_swap_b32_e32 v129, v135
	v_cndmask_b32_e64 v129, v129, v135, s[4:5]
	v_mul_f32 v135, v125, v128
	v_sub_f32 v145, v44, v43
	v_sub_f32 v146, v43, v42
	s_nop 0
	v_mul_f32 v129, v135, v129
	v_mov_b32_e32 v135, v127
	s_nop 1
	v_permlane32_swap_b32_e32 v128, v135
	v_cndmask_b32_e64 v128, v128, v135, s[4:5]
	v_mul_f32 v135, v125, v127
	v_mul_f32 v52, v52, v129
	v_mul_f32 v50, v50, v129
	v_mul_f32 v51, v51, v129
	s_nop 0
	v_mul_f32 v128, v135, v128
	v_mov_b32_e32 v135, v62
	s_nop 1
	v_permlane32_swap_b32_e32 v127, v135
	v_cndmask_b32_e64 v127, v127, v135, s[4:5]
	v_mul_f32 v135, v125, v62
	v_sub_f32 v139, v51, v50
	v_mul_f32 v50, v56, v128
	v_sub_f32 v138, v52, v51
	v_mul_f32 v51, v55, v128
	s_nop 0
	v_mul_f32 v135, v135, v127
	v_mov_b32_e32 v127, v62
	s_nop 1
	v_permlane32_swap_b32_e32 v127, v136
	v_cndmask_b32_e64 v127, v127, v136, s[4:5]
	v_mul_f32 v136, v125, v127
	v_mov_b32_e32 v127, v133
	s_nop 1
	v_permlane32_swap_b32_e32 v127, v137
	v_cndmask_b32_e64 v127, v127, v137, s[4:5]
	v_mul_f32 v127, v133, v127
	v_sub_f32 v133, v134, v37
	v_sub_f32 v37, v37, v36
	v_sub_f32 v36, v36, v35
	v_mul_f32 v35, v53, v129
	v_mul_f32 v42, v60, v135
	v_mul_f32 v43, v59, v135
	v_sub_f32 v141, v50, v51
	s_nop 0
	v_mul_f32 v127, v125, v127
	v_sub_f32 v134, v129, v35
	v_sub_f32 v137, v35, v52
	v_mul_f32 v35, v41, v132
	v_sub_f32 v148, v42, v43
	v_mul_f32 v52, v54, v128
	v_cvt_pk_bf16_f32 v129, v37, v133
	v_sub_f32 v41, v132, v35
	v_sub_f32 v35, v35, v40
	v_sub_f32 v40, v40, v39
	v_mul_f32 v39, v57, v128
	v_sub_f32 v142, v51, v52
	s_nop 0
	v_sub_f32 v132, v128, v39
	v_sub_f32 v140, v39, v50
	v_mul_f32 v39, v45, v131
	v_cvt_pk_bf16_f32 v128, v34, v36
	v_sub_f32 v143, v131, v39
	v_sub_f32 v144, v39, v44
	v_mul_f32 v39, v61, v135
	v_mul_f32 v44, v58, v135
	v_cvt_pk_bf16_f32 v131, v35, v41
	v_sub_f32 v135, v135, v39
	v_sub_f32 v147, v39, v42
	v_sub_f32 v149, v43, v44
	v_mul_f32 v39, v49, v130
	v_mul_f32 v42, v48, v130
	v_mul_f32 v43, v47, v130
	v_mul_f32 v44, v46, v130
	s_nop 0
	v_sub_f32 v150, v130, v39
	v_sub_f32 v151, v39, v42
	v_sub_f32 v152, v42, v43
	v_sub_f32 v153, v43, v44
	v_mul_f32 v39, v65, v136
	v_mul_f32 v42, v64, v136
	v_mul_f32 v43, v63, v136
	v_mul_f32 v44, v62, v136
	v_cvt_pk_bf16_f32 v130, v38, v40
	v_sub_f32 v136, v136, v39
	v_sub_f32 v154, v39, v42
	v_sub_f32 v155, v42, v43
	v_sub_f32 v156, v43, v44
	s_nop 1
	v_mfma_f32_32x32x16_bf16 v[18:33], v[110:113], v[128:131], v[18:33]
	v_mfma_f32_32x32x16_bf16 v[2:17], v[106:109], v[128:131], v[2:17]
	v_cvt_pk_bf16_f32 v106, v146, v145
	v_cvt_pk_bf16_f32 v107, v144, v143
	v_cvt_pk_bf16_f32 v108, v153, v152
	v_cvt_pk_bf16_f32 v109, v151, v150
	s_nop 1
	v_mfma_f32_32x32x16_bf16 v[18:33], v[102:105], v[106:109], v[18:33]
	v_mfma_f32_32x32x16_bf16 v[2:17], v[98:101], v[106:109], v[2:17]
	v_cvt_pk_bf16_f32 v98, v139, v138
	v_cvt_pk_bf16_f32 v99, v137, v134
	v_cvt_pk_bf16_f32 v100, v142, v141
	v_cvt_pk_bf16_f32 v101, v140, v132
	s_nop 1
	v_mfma_f32_32x32x16_bf16 v[18:33], v[94:97], v[98:101], v[18:33]
	v_mfma_f32_32x32x16_bf16 v[2:17], v[90:93], v[98:101], v[2:17]
	v_cvt_pk_bf16_f32 v90, v149, v148
	v_cvt_pk_bf16_f32 v91, v147, v135
	v_cvt_pk_bf16_f32 v92, v156, v155
	v_cvt_pk_bf16_f32 v93, v154, v136
	s_nop 1
	v_mfma_f32_32x32x16_bf16 v[18:33], v[86:89], v[90:93], v[18:33]
	v_mfma_f32_32x32x16_bf16 v[2:17], v[82:85], v[90:93], v[2:17]
	v_mov_b32_e32 v125, v127
	s_branch .LBB0_887
